# SwiGLU epilogue: LDS-table wait moved to its first consumer (the scalar address set-up overlaps the table reads' latency)
# baseline (speedup 1.0000x reference)
; __device__ __forceinline__ unsigned cvt_pk_bf16(float lo, float hi) { const f32x2_t v = {lo, hi}; const bf16x2_t b = __builtin_convertvector(v, bf16x2_t); return __builtin_bit_cast(unsigned, b); }
;     __device__ __forceinline__ void operator()(const f32x4 (&acc)[2][2][4][2], const Unit& u, int wr, int wc, int fr, int fq, int ui) const {
;         const int cb = u.pn * BM + wc * 32 + 8 * fq, jcol = u.pn * HALF + wc * 32 + 8 * fq;
;         (void)cb;
;         f32x4 bg[2], bu[2];
;         const float* bt = btab + ui * 256 + wc * 32 + 8 * fq;
; #pragma unroll
;         for (int n = 0; n < 2; ++n) { bg[n] = *(const f32x4*)(bt + 4 * n); bu[n] = *(const f32x4*)(bt + HALF + 4 * n); }
;         float rs[2][4];
; #pragma unroll
;         for (int ai = 0; ai < 2; ++ai)
; #pragma unroll
;             for (int m = 0; m < 4; ++m) rs[ai][m] = rtab[ui * 256 + ai * HALF + wr * 64 + m * 16 + fr];
; #pragma unroll
;         for (int ai = 0; ai < 2; ++ai)
; #pragma unroll
;             for (int m = 0; m < 4; ++m) {
;                 const float r = rs[ai][m]; const int row = u.pm * BM + ai * HALF + wr * 64 + m * 16 + fr;
;                 float g[8], v[8], e[8];
; #pragma unroll
;                 for (int n = 0; n < 2; ++n)
; #pragma unroll
;                     for (int i = 0; i < 4; ++i) { g[n * 4 + i] = fmaf(acc[ai][0][m][n][i], r, bg[n][i]); v[n * 4 + i] = fmaf(acc[ai][1][m][n][i], r, bu[n][i]); }
; #pragma unroll
;                 for (int i = 0; i < 8; ++i) e[i] = __builtin_amdgcn_exp2f(g[i] * (-LOG2E));
; #pragma unroll
;                 for (int i = 0; i < 8; ++i) e[i] = __builtin_amdgcn_rcpf(1.0f + e[i]);
; #pragma unroll
;                 for (int i = 0; i < 8; ++i) e[i] = (g[i] * e[i]) * v[i];
;                 u32x4 w; w.x = cvt_pk_bf16(e[0], e[1]); w.y = cvt_pk_bf16(e[2], e[3]); w.z = cvt_pk_bf16(e[4], e[5]); w.w = cvt_pk_bf16(e[6], e[7]);
;                 *(u32x4*)(act + ((size_t)((row >> 8) * (F / 64) + (jcol >> 6)) * 256 + (row & 255)) * 64 + (jcol & 63)) = w;
.LBB0_249:
	v_lshl_add_u32 v162, s56, 8, v171
	v_lshl_add_u32 v162, v162, 2, 0
	v_lshl_add_u32 v84, s56, 10, v179
	v_add_u32_e32 v162, 0x22000, v162
	ds_read_b128 v[96:99], v84
	ds_read_b128 v[80:83], v84 offset:16
	ds_read_b128 v[100:103], v84 offset:512
	ds_read_b128 v[84:87], v84 offset:528
	ds_read2_b32 v[166:167], v162 offset1:16
	ds_read2_b32 v[176:177], v162 offset0:32 offset1:48
	ds_read2_b32 v[164:165], v162 offset0:128 offset1:144
	ds_read2_b32 v[162:163], v162 offset0:160 offset1:176
	s_lshl_b32 s11, s55, 8
	v_mov_b32_e32 v222, 0xbfb8aa3b
	v_mov_b32_e32 v224, 1.0
	s_lshl_b32 s9, s57, 7
	s_add_i32 s16, s11, s49
	s_or_b32 s9, s9, s50
	s_ashr_i32 s16, s16, 8
	s_ashr_i32 s9, s9, 6
	s_mulk_i32 s16, 0x58
	s_add_i32 s16, s16, s9
	s_ashr_i32 s17, s16, 31
	s_lshl_b64 s[16:17], s[16:17], 15
	s_add_u32 s16, s16, 0x1000
	s_addc_u32 s17, s17, 0
	v_lshl_add_u64 v[214:215], v[154:155], 0, s[16:17]
	v_lshl_add_u64 v[214:215], v[214:215], 0, v[128:129]
	s_add_i32 s11, s11, s53
	s_ashr_i32 s11, s11, 8
	s_mulk_i32 s11, 0x58
	s_add_i32 s16, s11, s9
	s_ashr_i32 s17, s16, 31
	s_lshl_b64 s[16:17], s[16:17], 15
	s_add_u32 s16, s16, 0x1000
	s_addc_u32 s17, s17, 0
	v_lshl_add_u64 v[216:217], v[156:157], 0, s[16:17]
	v_lshl_add_u64 v[216:217], v[216:217], 0, v[128:129]
	s_mov_b64 s[16:17], -1
	s_movk_i32 s18, 0x1000
	s_mov_b32 s65, s67
	s_waitcnt lgkmcnt(0)
	v_pk_fma_f32 v[142:143], v[142:143], v[166:167], v[96:97] op_sel_hi:[1,0,1]
	v_pk_fma_f32 v[144:145], v[144:145], v[166:167], v[98:99] op_sel_hi:[1,0,1]
	v_pk_fma_f32 v[134:135], v[134:135], v[166:167], v[80:81] op_sel_hi:[1,0,1]
	v_pk_fma_f32 v[136:137], v[136:137], v[166:167], v[82:83] op_sel_hi:[1,0,1]
	v_pk_mul_f32 v[198:199], v[142:143], v[222:223] op_sel_hi:[1,0]
	v_pk_mul_f32 v[200:201], v[144:145], v[222:223] op_sel_hi:[1,0]
	v_pk_mul_f32 v[202:203], v[134:135], v[222:223] op_sel_hi:[1,0]
	v_pk_mul_f32 v[204:205], v[136:137], v[222:223] op_sel_hi:[1,0]
	v_pk_fma_f32 v[138:139], v[138:139], v[166:167], v[100:101] op_sel_hi:[1,0,1]
	v_pk_fma_f32 v[140:141], v[140:141], v[166:167], v[102:103] op_sel_hi:[1,0,1]
	v_pk_fma_f32 v[130:131], v[130:131], v[166:167], v[84:85] op_sel_hi:[1,0,1]
	v_pk_fma_f32 v[132:133], v[132:133], v[166:167], v[86:87] op_sel_hi:[1,0,1]
	v_exp_f32_e32 v198, v198
	v_exp_f32_e32 v199, v199
	v_exp_f32_e32 v200, v200
	v_exp_f32_e32 v201, v201
	v_exp_f32_e32 v202, v202
	v_exp_f32_e32 v203, v203
	v_exp_f32_e32 v204, v204
	v_exp_f32_e32 v205, v205
	v_pk_add_f32 v[198:199], v[198:199], v[224:225] op_sel_hi:[1,0]
	v_pk_add_f32 v[200:201], v[200:201], v[224:225] op_sel_hi:[1,0]
	v_pk_add_f32 v[202:203], v[202:203], v[224:225] op_sel_hi:[1,0]
	v_pk_add_f32 v[204:205], v[204:205], v[224:225] op_sel_hi:[1,0]
	v_rcp_f32_e32 v198, v198
	v_rcp_f32_e32 v199, v199
	v_rcp_f32_e32 v200, v200
	v_rcp_f32_e32 v201, v201
	v_rcp_f32_e32 v202, v202
	v_rcp_f32_e32 v203, v203
	v_rcp_f32_e32 v204, v204
	v_rcp_f32_e32 v205, v205
	v_pk_mul_f32 v[142:143], v[142:143], v[198:199]
	v_pk_mul_f32 v[144:145], v[144:145], v[200:201]
	v_pk_mul_f32 v[134:135], v[134:135], v[202:203]
	v_pk_mul_f32 v[136:137], v[136:137], v[204:205]
	v_pk_mul_f32 v[142:143], v[138:139], v[142:143]
	v_pk_mul_f32 v[144:145], v[140:141], v[144:145]
	v_pk_mul_f32 v[134:135], v[130:131], v[134:135]
	v_pk_mul_f32 v[136:137], v[132:133], v[136:137]
	v_cvt_pk_bf16_f32 v206, v142, v143
	v_cvt_pk_bf16_f32 v207, v144, v145
	v_cvt_pk_bf16_f32 v208, v134, v135
	v_cvt_pk_bf16_f32 v209, v136, v137
	global_store_dwordx4 v[214:215], v[206:209], off offset:-4096
	v_pk_fma_f32 v[124:125], v[124:125], v[166:167], v[96:97] op_sel:[0,1,0]
	v_pk_fma_f32 v[126:127], v[126:127], v[166:167], v[98:99] op_sel:[0,1,0]
	v_pk_fma_f32 v[116:117], v[116:117], v[166:167], v[80:81] op_sel:[0,1,0]
	v_pk_fma_f32 v[118:119], v[118:119], v[166:167], v[82:83] op_sel:[0,1,0]
	v_pk_mul_f32 v[198:199], v[124:125], v[222:223] op_sel_hi:[1,0]
	v_pk_mul_f32 v[200:201], v[126:127], v[222:223] op_sel_hi:[1,0]
	v_pk_mul_f32 v[202:203], v[116:117], v[222:223] op_sel_hi:[1,0]
	v_pk_mul_f32 v[204:205], v[118:119], v[222:223] op_sel_hi:[1,0]
	v_pk_fma_f32 v[120:121], v[120:121], v[166:167], v[100:101] op_sel:[0,1,0]
	v_pk_fma_f32 v[122:123], v[122:123], v[166:167], v[102:103] op_sel:[0,1,0]
	v_pk_fma_f32 v[112:113], v[112:113], v[166:167], v[84:85] op_sel:[0,1,0]
	v_pk_fma_f32 v[114:115], v[114:115], v[166:167], v[86:87] op_sel:[0,1,0]
	v_exp_f32_e32 v198, v198
	v_exp_f32_e32 v199, v199
	v_exp_f32_e32 v200, v200
	v_exp_f32_e32 v201, v201
	v_exp_f32_e32 v202, v202
	v_exp_f32_e32 v203, v203
	v_exp_f32_e32 v204, v204
	v_exp_f32_e32 v205, v205
	v_pk_add_f32 v[198:199], v[198:199], v[224:225] op_sel_hi:[1,0]
	v_pk_add_f32 v[200:201], v[200:201], v[224:225] op_sel_hi:[1,0]
	v_pk_add_f32 v[202:203], v[202:203], v[224:225] op_sel_hi:[1,0]
	v_pk_add_f32 v[204:205], v[204:205], v[224:225] op_sel_hi:[1,0]
	v_rcp_f32_e32 v198, v198
	v_rcp_f32_e32 v199, v199
	v_rcp_f32_e32 v200, v200
	v_rcp_f32_e32 v201, v201
	v_rcp_f32_e32 v202, v202
	v_rcp_f32_e32 v203, v203
	v_rcp_f32_e32 v204, v204
	v_rcp_f32_e32 v205, v205
	v_pk_mul_f32 v[124:125], v[124:125], v[198:199]
	v_pk_mul_f32 v[126:127], v[126:127], v[200:201]
	v_pk_mul_f32 v[116:117], v[116:117], v[202:203]
	v_pk_mul_f32 v[118:119], v[118:119], v[204:205]
	v_pk_mul_f32 v[124:125], v[120:121], v[124:125]
	v_pk_mul_f32 v[126:127], v[122:123], v[126:127]
	v_pk_mul_f32 v[116:117], v[112:113], v[116:117]
	v_pk_mul_f32 v[118:119], v[114:115], v[118:119]
	v_cvt_pk_bf16_f32 v210, v124, v125
	v_cvt_pk_bf16_f32 v211, v126, v127
	v_cvt_pk_bf16_f32 v212, v116, v117
	v_cvt_pk_bf16_f32 v213, v118, v119
	global_store_dwordx4 v[214:215], v[210:213], off offset:-2048
; __device__ __forceinline__ unsigned cvt_pk_bf16(float lo, float hi) { const f32x2_t v = {lo, hi}; const bf16x2_t b = __builtin_convertvector(v, bf16x2_t); return __builtin_bit_cast(unsigned, b); }
;     __device__ __forceinline__ void operator()(const f32x4 (&acc)[2][2][4][2], const Unit& u, int wr, int wc, int fr, int fq, int ui) const {
;     ...
;         for (int ai = 0; ai < 2; ++ai)
; #pragma unroll
;             for (int m = 0; m < 4; ++m) {
;                 const float r = rs[ai][m]; const int row = u.pm * BM + ai * HALF + wr * 64 + m * 16 + fr;
;                 float g[8], v[8], e[8];
; #pragma unroll
;                 for (int n = 0; n < 2; ++n)
; #pragma unroll
;                     for (int i = 0; i < 4; ++i) { g[n * 4 + i] = fmaf(acc[ai][0][m][n][i], r, bg[n][i]); v[n * 4 + i] = fmaf(acc[ai][1][m][n][i], r, bu[n][i]); }
; #pragma unroll
;                 for (int i = 0; i < 8; ++i) e[i] = __builtin_amdgcn_exp2f(g[i] * (-LOG2E));
; #pragma unroll
;                 for (int i = 0; i < 8; ++i) e[i] = __builtin_amdgcn_rcpf(1.0f + e[i]);
; #pragma unroll
;                 for (int i = 0; i < 8; ++i) e[i] = (g[i] * e[i]) * v[i];
;                 u32x4 w; w.x = cvt_pk_bf16(e[0], e[1]); w.y = cvt_pk_bf16(e[2], e[3]); w.z = cvt_pk_bf16(e[4], e[5]); w.w = cvt_pk_bf16(e[6], e[7]);
;                 *(u32x4*)(act + ((size_t)((row >> 8) * (F / 64) + (jcol >> 6)) * 256 + (row & 255)) * 64 + (jcol & 63)) = w;
	v_pk_fma_f32 v[108:109], v[108:109], v[176:177], v[96:97] op_sel_hi:[1,0,1]
	v_pk_fma_f32 v[110:111], v[110:111], v[176:177], v[98:99] op_sel_hi:[1,0,1]
	v_pk_fma_f32 v[92:93], v[92:93], v[176:177], v[80:81] op_sel_hi:[1,0,1]
	v_pk_fma_f32 v[94:95], v[94:95], v[176:177], v[82:83] op_sel_hi:[1,0,1]
	v_pk_mul_f32 v[198:199], v[108:109], v[222:223] op_sel_hi:[1,0]
	v_pk_mul_f32 v[200:201], v[110:111], v[222:223] op_sel_hi:[1,0]
	v_pk_mul_f32 v[202:203], v[92:93], v[222:223] op_sel_hi:[1,0]
	v_pk_mul_f32 v[204:205], v[94:95], v[222:223] op_sel_hi:[1,0]
	v_pk_fma_f32 v[104:105], v[104:105], v[176:177], v[100:101] op_sel_hi:[1,0,1]
	v_pk_fma_f32 v[106:107], v[106:107], v[176:177], v[102:103] op_sel_hi:[1,0,1]
	v_pk_fma_f32 v[88:89], v[88:89], v[176:177], v[84:85] op_sel_hi:[1,0,1]
	v_pk_fma_f32 v[90:91], v[90:91], v[176:177], v[86:87] op_sel_hi:[1,0,1]
	v_exp_f32_e32 v198, v198
	v_exp_f32_e32 v199, v199
	v_exp_f32_e32 v200, v200
	v_exp_f32_e32 v201, v201
	v_exp_f32_e32 v202, v202
	v_exp_f32_e32 v203, v203
	v_exp_f32_e32 v204, v204
	v_exp_f32_e32 v205, v205
	v_pk_add_f32 v[198:199], v[198:199], v[224:225] op_sel_hi:[1,0]
	v_pk_add_f32 v[200:201], v[200:201], v[224:225] op_sel_hi:[1,0]
	v_pk_add_f32 v[202:203], v[202:203], v[224:225] op_sel_hi:[1,0]
	v_pk_add_f32 v[204:205], v[204:205], v[224:225] op_sel_hi:[1,0]
	v_rcp_f32_e32 v198, v198
	v_rcp_f32_e32 v199, v199
	v_rcp_f32_e32 v200, v200
	v_rcp_f32_e32 v201, v201
	v_rcp_f32_e32 v202, v202
	v_rcp_f32_e32 v203, v203
	v_rcp_f32_e32 v204, v204
	v_rcp_f32_e32 v205, v205
	v_pk_mul_f32 v[108:109], v[108:109], v[198:199]
	v_pk_mul_f32 v[110:111], v[110:111], v[200:201]
	v_pk_mul_f32 v[92:93], v[92:93], v[202:203]
	v_pk_mul_f32 v[94:95], v[94:95], v[204:205]
	v_pk_mul_f32 v[108:109], v[104:105], v[108:109]
	v_pk_mul_f32 v[110:111], v[106:107], v[110:111]
	v_pk_mul_f32 v[92:93], v[88:89], v[92:93]
	v_pk_mul_f32 v[94:95], v[90:91], v[94:95]
	v_cvt_pk_bf16_f32 v206, v108, v109
	v_cvt_pk_bf16_f32 v207, v110, v111
	v_cvt_pk_bf16_f32 v208, v92, v93
	v_cvt_pk_bf16_f32 v209, v94, v95
	global_store_dwordx4 v[214:215], v[206:209], off
	v_pk_fma_f32 v[76:77], v[76:77], v[176:177], v[96:97] op_sel:[0,1,0]
	v_pk_fma_f32 v[78:79], v[78:79], v[176:177], v[98:99] op_sel:[0,1,0]
	v_pk_fma_f32 v[68:69], v[68:69], v[176:177], v[80:81] op_sel:[0,1,0]
	v_pk_fma_f32 v[70:71], v[70:71], v[176:177], v[82:83] op_sel:[0,1,0]
	v_pk_mul_f32 v[198:199], v[76:77], v[222:223] op_sel_hi:[1,0]
	v_pk_mul_f32 v[200:201], v[78:79], v[222:223] op_sel_hi:[1,0]
	v_pk_mul_f32 v[202:203], v[68:69], v[222:223] op_sel_hi:[1,0]
	v_pk_mul_f32 v[204:205], v[70:71], v[222:223] op_sel_hi:[1,0]
	v_pk_fma_f32 v[72:73], v[72:73], v[176:177], v[100:101] op_sel:[0,1,0]
	v_pk_fma_f32 v[74:75], v[74:75], v[176:177], v[102:103] op_sel:[0,1,0]
	v_pk_fma_f32 v[64:65], v[64:65], v[176:177], v[84:85] op_sel:[0,1,0]
	v_pk_fma_f32 v[66:67], v[66:67], v[176:177], v[86:87] op_sel:[0,1,0]
	v_exp_f32_e32 v198, v198
	v_exp_f32_e32 v199, v199
	v_exp_f32_e32 v200, v200
	v_exp_f32_e32 v201, v201
	v_exp_f32_e32 v202, v202
	v_exp_f32_e32 v203, v203
	v_exp_f32_e32 v204, v204
	v_exp_f32_e32 v205, v205
	v_pk_add_f32 v[198:199], v[198:199], v[224:225] op_sel_hi:[1,0]
	v_pk_add_f32 v[200:201], v[200:201], v[224:225] op_sel_hi:[1,0]
	v_pk_add_f32 v[202:203], v[202:203], v[224:225] op_sel_hi:[1,0]
	v_pk_add_f32 v[204:205], v[204:205], v[224:225] op_sel_hi:[1,0]
	v_rcp_f32_e32 v198, v198
	v_rcp_f32_e32 v199, v199
	v_rcp_f32_e32 v200, v200
	v_rcp_f32_e32 v201, v201
	v_rcp_f32_e32 v202, v202
	v_rcp_f32_e32 v203, v203
	v_rcp_f32_e32 v204, v204
	v_rcp_f32_e32 v205, v205
	v_pk_mul_f32 v[76:77], v[76:77], v[198:199]
	v_pk_mul_f32 v[78:79], v[78:79], v[200:201]
	v_pk_mul_f32 v[68:69], v[68:69], v[202:203]
	v_pk_mul_f32 v[70:71], v[70:71], v[204:205]
	v_pk_mul_f32 v[76:77], v[72:73], v[76:77]
	v_pk_mul_f32 v[78:79], v[74:75], v[78:79]
	v_pk_mul_f32 v[68:69], v[64:65], v[68:69]
	v_pk_mul_f32 v[70:71], v[66:67], v[70:71]
	v_cvt_pk_bf16_f32 v210, v76, v77
	v_cvt_pk_bf16_f32 v211, v78, v79
	v_cvt_pk_bf16_f32 v212, v68, v69
	v_cvt_pk_bf16_f32 v213, v70, v71
	global_store_dwordx4 v[214:215], v[210:213], off offset:2048
	v_pk_fma_f32 v[60:61], v[60:61], v[164:165], v[96:97] op_sel_hi:[1,0,1]
	v_pk_fma_f32 v[62:63], v[62:63], v[164:165], v[98:99] op_sel_hi:[1,0,1]
	v_pk_fma_f32 v[52:53], v[52:53], v[164:165], v[80:81] op_sel_hi:[1,0,1]
	v_pk_fma_f32 v[54:55], v[54:55], v[164:165], v[82:83] op_sel_hi:[1,0,1]
	v_pk_mul_f32 v[198:199], v[60:61], v[222:223] op_sel_hi:[1,0]
	v_pk_mul_f32 v[200:201], v[62:63], v[222:223] op_sel_hi:[1,0]
	v_pk_mul_f32 v[202:203], v[52:53], v[222:223] op_sel_hi:[1,0]
	v_pk_mul_f32 v[204:205], v[54:55], v[222:223] op_sel_hi:[1,0]
	v_pk_fma_f32 v[56:57], v[56:57], v[164:165], v[100:101] op_sel_hi:[1,0,1]
	v_pk_fma_f32 v[58:59], v[58:59], v[164:165], v[102:103] op_sel_hi:[1,0,1]
	v_pk_fma_f32 v[48:49], v[48:49], v[164:165], v[84:85] op_sel_hi:[1,0,1]
	v_pk_fma_f32 v[50:51], v[50:51], v[164:165], v[86:87] op_sel_hi:[1,0,1]
	v_exp_f32_e32 v198, v198
	v_exp_f32_e32 v199, v199
	v_exp_f32_e32 v200, v200
	v_exp_f32_e32 v201, v201
	v_exp_f32_e32 v202, v202
	v_exp_f32_e32 v203, v203
	v_exp_f32_e32 v204, v204
	v_exp_f32_e32 v205, v205
	v_pk_add_f32 v[198:199], v[198:199], v[224:225] op_sel_hi:[1,0]
	v_pk_add_f32 v[200:201], v[200:201], v[224:225] op_sel_hi:[1,0]
	v_pk_add_f32 v[202:203], v[202:203], v[224:225] op_sel_hi:[1,0]
	v_pk_add_f32 v[204:205], v[204:205], v[224:225] op_sel_hi:[1,0]
	v_rcp_f32_e32 v198, v198
	v_rcp_f32_e32 v199, v199
	v_rcp_f32_e32 v200, v200
	v_rcp_f32_e32 v201, v201
	v_rcp_f32_e32 v202, v202
	v_rcp_f32_e32 v203, v203
	v_rcp_f32_e32 v204, v204
; __device__ __forceinline__ unsigned cvt_pk_bf16(float lo, float hi) { const f32x2_t v = {lo, hi}; const bf16x2_t b = __builtin_convertvector(v, bf16x2_t); return __builtin_bit_cast(unsigned, b); }
;     __device__ __forceinline__ void operator()(const f32x4 (&acc)[2][2][4][2], const Unit& u, int wr, int wc, int fr, int fq, int ui) const {
;     ...
;         for (int ai = 0; ai < 2; ++ai)
; #pragma unroll
;             for (int m = 0; m < 4; ++m) {
;                 const float r = rs[ai][m]; const int row = u.pm * BM + ai * HALF + wr * 64 + m * 16 + fr;
;                 float g[8], v[8], e[8];
; #pragma unroll
;                 for (int n = 0; n < 2; ++n)
; #pragma unroll
;                     for (int i = 0; i < 4; ++i) { g[n * 4 + i] = fmaf(acc[ai][0][m][n][i], r, bg[n][i]); v[n * 4 + i] = fmaf(acc[ai][1][m][n][i], r, bu[n][i]); }
; #pragma unroll
;                 for (int i = 0; i < 8; ++i) e[i] = __builtin_amdgcn_exp2f(g[i] * (-LOG2E));
; #pragma unroll
;                 for (int i = 0; i < 8; ++i) e[i] = __builtin_amdgcn_rcpf(1.0f + e[i]);
; #pragma unroll
;                 for (int i = 0; i < 8; ++i) e[i] = (g[i] * e[i]) * v[i];
;                 u32x4 w; w.x = cvt_pk_bf16(e[0], e[1]); w.y = cvt_pk_bf16(e[2], e[3]); w.z = cvt_pk_bf16(e[4], e[5]); w.w = cvt_pk_bf16(e[6], e[7]);
;                 *(u32x4*)(act + ((size_t)((row >> 8) * (F / 64) + (jcol >> 6)) * 256 + (row & 255)) * 64 + (jcol & 63)) = w;
	v_rcp_f32_e32 v205, v205
	v_pk_mul_f32 v[60:61], v[60:61], v[198:199]
	v_pk_mul_f32 v[62:63], v[62:63], v[200:201]
	v_pk_mul_f32 v[52:53], v[52:53], v[202:203]
	v_pk_mul_f32 v[54:55], v[54:55], v[204:205]
	v_pk_mul_f32 v[60:61], v[56:57], v[60:61]
	v_pk_mul_f32 v[62:63], v[58:59], v[62:63]
	v_pk_mul_f32 v[52:53], v[48:49], v[52:53]
	v_pk_mul_f32 v[54:55], v[50:51], v[54:55]
	v_cvt_pk_bf16_f32 v206, v60, v61
	v_cvt_pk_bf16_f32 v207, v62, v63
	v_cvt_pk_bf16_f32 v208, v52, v53
	v_cvt_pk_bf16_f32 v209, v54, v55
	global_store_dwordx4 v[216:217], v[206:209], off offset:-4096
	v_pk_fma_f32 v[44:45], v[44:45], v[164:165], v[96:97] op_sel:[0,1,0]
	v_pk_fma_f32 v[46:47], v[46:47], v[164:165], v[98:99] op_sel:[0,1,0]
	v_pk_fma_f32 v[36:37], v[36:37], v[164:165], v[80:81] op_sel:[0,1,0]
	v_pk_fma_f32 v[38:39], v[38:39], v[164:165], v[82:83] op_sel:[0,1,0]
	v_pk_mul_f32 v[198:199], v[44:45], v[222:223] op_sel_hi:[1,0]
	v_pk_mul_f32 v[200:201], v[46:47], v[222:223] op_sel_hi:[1,0]
	v_pk_mul_f32 v[202:203], v[36:37], v[222:223] op_sel_hi:[1,0]
	v_pk_mul_f32 v[204:205], v[38:39], v[222:223] op_sel_hi:[1,0]
	v_pk_fma_f32 v[40:41], v[40:41], v[164:165], v[100:101] op_sel:[0,1,0]
	v_pk_fma_f32 v[42:43], v[42:43], v[164:165], v[102:103] op_sel:[0,1,0]
	v_pk_fma_f32 v[32:33], v[32:33], v[164:165], v[84:85] op_sel:[0,1,0]
	v_pk_fma_f32 v[34:35], v[34:35], v[164:165], v[86:87] op_sel:[0,1,0]
	v_exp_f32_e32 v198, v198
	v_exp_f32_e32 v199, v199
	v_exp_f32_e32 v200, v200
	v_exp_f32_e32 v201, v201
	v_exp_f32_e32 v202, v202
	v_exp_f32_e32 v203, v203
	v_exp_f32_e32 v204, v204
	v_exp_f32_e32 v205, v205
	v_pk_add_f32 v[198:199], v[198:199], v[224:225] op_sel_hi:[1,0]
	v_pk_add_f32 v[200:201], v[200:201], v[224:225] op_sel_hi:[1,0]
	v_pk_add_f32 v[202:203], v[202:203], v[224:225] op_sel_hi:[1,0]
	v_pk_add_f32 v[204:205], v[204:205], v[224:225] op_sel_hi:[1,0]
	v_rcp_f32_e32 v198, v198
	v_rcp_f32_e32 v199, v199
	v_rcp_f32_e32 v200, v200
	v_rcp_f32_e32 v201, v201
	v_rcp_f32_e32 v202, v202
	v_rcp_f32_e32 v203, v203
	v_rcp_f32_e32 v204, v204
	v_rcp_f32_e32 v205, v205
	v_pk_mul_f32 v[44:45], v[44:45], v[198:199]
	v_pk_mul_f32 v[46:47], v[46:47], v[200:201]
	v_pk_mul_f32 v[36:37], v[36:37], v[202:203]
	v_pk_mul_f32 v[38:39], v[38:39], v[204:205]
	v_pk_mul_f32 v[44:45], v[40:41], v[44:45]
	v_pk_mul_f32 v[46:47], v[42:43], v[46:47]
	v_pk_mul_f32 v[36:37], v[32:33], v[36:37]
	v_pk_mul_f32 v[38:39], v[34:35], v[38:39]
	v_cvt_pk_bf16_f32 v210, v44, v45
	v_cvt_pk_bf16_f32 v211, v46, v47
	v_cvt_pk_bf16_f32 v212, v36, v37
	v_cvt_pk_bf16_f32 v213, v38, v39
	global_store_dwordx4 v[216:217], v[210:213], off offset:-2048
	v_pk_fma_f32 v[28:29], v[28:29], v[162:163], v[96:97] op_sel_hi:[1,0,1]
	v_pk_fma_f32 v[30:31], v[30:31], v[162:163], v[98:99] op_sel_hi:[1,0,1]
	v_pk_fma_f32 v[20:21], v[20:21], v[162:163], v[80:81] op_sel_hi:[1,0,1]
	v_pk_fma_f32 v[22:23], v[22:23], v[162:163], v[82:83] op_sel_hi:[1,0,1]
	v_pk_mul_f32 v[198:199], v[28:29], v[222:223] op_sel_hi:[1,0]
	v_pk_mul_f32 v[200:201], v[30:31], v[222:223] op_sel_hi:[1,0]
	v_pk_mul_f32 v[202:203], v[20:21], v[222:223] op_sel_hi:[1,0]
	v_pk_mul_f32 v[204:205], v[22:23], v[222:223] op_sel_hi:[1,0]
	v_pk_fma_f32 v[24:25], v[24:25], v[162:163], v[100:101] op_sel_hi:[1,0,1]
	v_pk_fma_f32 v[26:27], v[26:27], v[162:163], v[102:103] op_sel_hi:[1,0,1]
	v_pk_fma_f32 v[16:17], v[16:17], v[162:163], v[84:85] op_sel_hi:[1,0,1]
	v_pk_fma_f32 v[18:19], v[18:19], v[162:163], v[86:87] op_sel_hi:[1,0,1]
	v_exp_f32_e32 v198, v198
	v_exp_f32_e32 v199, v199
	v_exp_f32_e32 v200, v200
	v_exp_f32_e32 v201, v201
	v_exp_f32_e32 v202, v202
	v_exp_f32_e32 v203, v203
	v_exp_f32_e32 v204, v204
	v_exp_f32_e32 v205, v205
	v_pk_add_f32 v[198:199], v[198:199], v[224:225] op_sel_hi:[1,0]
	v_pk_add_f32 v[200:201], v[200:201], v[224:225] op_sel_hi:[1,0]
	v_pk_add_f32 v[202:203], v[202:203], v[224:225] op_sel_hi:[1,0]
	v_pk_add_f32 v[204:205], v[204:205], v[224:225] op_sel_hi:[1,0]
	v_rcp_f32_e32 v198, v198
	v_rcp_f32_e32 v199, v199
	v_rcp_f32_e32 v200, v200
	v_rcp_f32_e32 v201, v201
	v_rcp_f32_e32 v202, v202
	v_rcp_f32_e32 v203, v203
	v_rcp_f32_e32 v204, v204
	v_rcp_f32_e32 v205, v205
	v_pk_mul_f32 v[28:29], v[28:29], v[198:199]
	v_pk_mul_f32 v[30:31], v[30:31], v[200:201]
	v_pk_mul_f32 v[20:21], v[20:21], v[202:203]
	v_pk_mul_f32 v[22:23], v[22:23], v[204:205]
	v_pk_mul_f32 v[28:29], v[24:25], v[28:29]
	v_pk_mul_f32 v[30:31], v[26:27], v[30:31]
	v_pk_mul_f32 v[20:21], v[16:17], v[20:21]
	v_pk_mul_f32 v[22:23], v[18:19], v[22:23]
	v_cvt_pk_bf16_f32 v206, v28, v29
	v_cvt_pk_bf16_f32 v207, v30, v31
	v_cvt_pk_bf16_f32 v208, v20, v21
	v_cvt_pk_bf16_f32 v209, v22, v23
	global_store_dwordx4 v[216:217], v[206:209], off
	v_pk_fma_f32 v[12:13], v[12:13], v[162:163], v[96:97] op_sel:[0,1,0]
	v_pk_fma_f32 v[14:15], v[14:15], v[162:163], v[98:99] op_sel:[0,1,0]
	v_pk_fma_f32 v[4:5], v[4:5], v[162:163], v[80:81] op_sel:[0,1,0]
	v_pk_fma_f32 v[6:7], v[6:7], v[162:163], v[82:83] op_sel:[0,1,0]
	v_pk_mul_f32 v[198:199], v[12:13], v[222:223] op_sel_hi:[1,0]
	v_pk_mul_f32 v[200:201], v[14:15], v[222:223] op_sel_hi:[1,0]
	v_pk_mul_f32 v[202:203], v[4:5], v[222:223] op_sel_hi:[1,0]
	v_pk_mul_f32 v[204:205], v[6:7], v[222:223] op_sel_hi:[1,0]
	v_pk_fma_f32 v[8:9], v[8:9], v[162:163], v[100:101] op_sel:[0,1,0]
	v_pk_fma_f32 v[10:11], v[10:11], v[162:163], v[102:103] op_sel:[0,1,0]
	v_pk_fma_f32 v[0:1], v[0:1], v[162:163], v[84:85] op_sel:[0,1,0]
	v_pk_fma_f32 v[2:3], v[2:3], v[162:163], v[86:87] op_sel:[0,1,0]
	v_exp_f32_e32 v198, v198
	v_exp_f32_e32 v199, v199
	v_exp_f32_e32 v200, v200
	v_exp_f32_e32 v201, v201
	v_exp_f32_e32 v202, v202
	v_exp_f32_e32 v203, v203
	v_exp_f32_e32 v204, v204
	v_exp_f32_e32 v205, v205
	v_pk_add_f32 v[198:199], v[198:199], v[224:225] op_sel_hi:[1,0]
	v_pk_add_f32 v[200:201], v[200:201], v[224:225] op_sel_hi:[1,0]
	v_pk_add_f32 v[202:203], v[202:203], v[224:225] op_sel_hi:[1,0]
	v_pk_add_f32 v[204:205], v[204:205], v[224:225] op_sel_hi:[1,0]
	v_rcp_f32_e32 v198, v198
	v_rcp_f32_e32 v199, v199
	v_rcp_f32_e32 v200, v200
	v_rcp_f32_e32 v201, v201
	v_rcp_f32_e32 v202, v202
	v_rcp_f32_e32 v203, v203
	v_rcp_f32_e32 v204, v204
	v_rcp_f32_e32 v205, v205
	v_pk_mul_f32 v[12:13], v[12:13], v[198:199]
	v_pk_mul_f32 v[14:15], v[14:15], v[200:201]
	v_pk_mul_f32 v[4:5], v[4:5], v[202:203]
	v_pk_mul_f32 v[6:7], v[6:7], v[204:205]
	v_pk_mul_f32 v[12:13], v[8:9], v[12:13]
	v_pk_mul_f32 v[14:15], v[10:11], v[14:15]
	v_pk_mul_f32 v[4:5], v[0:1], v[4:5]
	v_pk_mul_f32 v[6:7], v[2:3], v[6:7]
	v_cvt_pk_bf16_f32 v210, v12, v13
	v_cvt_pk_bf16_f32 v211, v14, v15
	v_cvt_pk_bf16_f32 v212, v4, v5
	v_cvt_pk_bf16_f32 v213, v6, v7
	global_store_dwordx4 v[216:217], v[210:213], off offset:2048
	s_andn2_b64 vcc, exec, s[2:3]
	s_cbranch_vccnz .LBB0_242
	s_andn2_b64 vcc, exec, s[4:5]
	s_cbranch_vccnz .LBB0_241
	s_barrier
	s_branch .LBB0_241
